# speedup vs baseline: 1.0133x; 1.0133x over previous
_Z16sum_layer_kernelPKfS0_Pf:
	s_load_dwordx4 s[4:7], s[0:1], 0x0
	s_load_dwordx2 s[8:9], s[0:1], 0x10
	v_lshrrev_b32_e32 v42, 6, v0
	v_bfe_u32 v41, v0, 5, 1
	v_and_b32_e32 v40, 31, v0
	v_readfirstlane_b32 s23, v42
	v_and_b32_e32 v43, 7, v0
	v_bfe_u32 v44, v0, 3, 3
	s_lshl_b32 s3, s2, 12
	s_lshl_b32 s19, s2, 7
	s_lshl_b32 s23, s23, 12
	v_lshlrev_b32_e32 v1, 11, v41
	v_lshl_or_b32 v1, v40, 2, v1
	s_mov_b32 m0, s23
	v_lshrrev_b32_e32 v46, 1, v44
	v_xor_b32_e32 v46, v43, v46
	v_lshlrev_b32_e32 v46, 4, v46
	v_lshl_add_u32 v35, v44, 16, v46
	v_lshl_add_u32 v35, v42, 21, v35
	v_add_u32_e32 v35, s19, v35
	v_xor_b32_e32 v86, 64, v35
	s_mov_b32 s20, 0x7fc00
	s_mov_b32 s21, 0xff800
	s_mov_b32 s22, 0x17f400
	s_mov_b32 s14, 0x200000
	s_mov_b32 s15, 0x20000
	v_and_b32_e32 v45, 63, v0
	v_lshlrev_b32_e32 v37, 4, v45
	s_add_u32 s54, s23, 0x4000
	s_waitcnt lgkmcnt(0)
	s_mov_b32 s12, s6
	s_and_b32 s13, s7, 0xffff
	s_and_b32 s5, s5, 0xffff
	s_mov_b32 s6, 0x800000
	s_mov_b32 s7, s15
	s_mov_b32 m0, s54
	s_nop 0
	buffer_load_dwordx4 v37, s[12:15], s3 offen nt lds
	buffer_load_dwordx4 v37, s[12:15], s3 offen offset:1024 nt lds
	buffer_load_dwordx4 v37, s[12:15], s3 offen offset:2048 nt lds
	buffer_load_dwordx4 v37, s[12:15], s3 offen offset:3072 nt lds
	s_mov_b32 m0, s23
	s_nop 0
	buffer_load_dwordx4 v35, s[4:7], 0 offen nt lds
	buffer_load_dwordx4 v86, s[4:7], s20 offen offset:1024 nt lds
	buffer_load_dwordx4 v35, s[4:7], s21 offen offset:2048 nt lds
	buffer_load_dwordx4 v86, s[4:7], s22 offen offset:3072 nt lds
	v_and_b32_e32 v45, 63, v0
	v_lshlrev_b32_e32 v36, 2, v40
	v_lshl_add_u32 v36, v41, 18, v36
	v_lshl_add_u32 v36, v42, 21, v36
	v_add_u32_e32 v36, s19, v36
	v_bfe_u32 v47, v40, 1, 3
	v_lshlrev_b32_e32 v39, 2, v41
	v_xor_b32_e32 v39, v39, v47
	v_lshlrev_b32_e32 v39, 4, v39
	v_lshl_add_u32 v39, v40, 7, v39
	v_lshl_add_u32 v39, v42, 12, v39
	v_xor_b32_e32 v81, 16, v39
	v_xor_b32_e32 v82, 32, v39
	v_xor_b32_e32 v83, 48, v39
	v_cmp_gt_u32_e32 vcc, 32, v45
	v_mov_b32_e32 v34, 0xc1600000
	v_mov_b32_e32 v84, 0x3fb8aa3b
	v_mov_b32_e32 v85, 0x3f317218
	s_lshl_b32 s24, 1, 16
	s_lshl_b32 s25, 2, 16
	s_lshl_b32 s26, 3, 16
	s_lshl_b32 s27, 8, 16
	s_lshl_b32 s28, 9, 16
	s_lshl_b32 s29, 10, 16
	s_lshl_b32 s30, 11, 16
	s_lshl_b32 s31, 16, 16
	s_lshl_b32 s32, 17, 16
	s_lshl_b32 s33, 18, 16
	s_lshl_b32 s34, 19, 16
	s_lshl_b32 s35, 24, 16
	s_lshl_b32 s36, 25, 16
	s_lshl_b32 s37, 26, 16
	s_lshl_b32 s38, 27, 16
	s_and_b32 s9, s9, 0xffff
	s_mov_b32 s10, s6
	s_mov_b32 s11, s15
	v_lshl_add_u32 v38, v42, 12, v1
	v_add_u32_e32 v38, 0x4000, v38
	v_add_u32_e32 v87, 0x400, v38
	s_waitcnt vmcnt(4)
	ds_read2_b32 v[18:19], v38 offset0:0 offset1:32
	ds_read2_b32 v[20:21], v38 offset0:64 offset1:96
	ds_read2_b32 v[22:23], v38 offset0:128 offset1:160
	ds_read2_b32 v[24:25], v38 offset0:192 offset1:224
	ds_read2_b32 v[26:27], v87 offset0:0 offset1:32
	ds_read2_b32 v[28:29], v87 offset0:64 offset1:96
	ds_read2_b32 v[30:31], v87 offset0:128 offset1:160
	ds_read2_b32 v[32:33], v87 offset0:192 offset1:224
	s_waitcnt lgkmcnt(0)
	v_max3_f32 v48, v18, v19, v20
	v_max3_f32 v50, v21, v22, v23
	v_max3_f32 v48, v48, v24, v25
	v_max3_f32 v50, v50, v26, v27
	v_max3_f32 v48, v48, v28, v29
	v_max3_f32 v50, v50, v30, v31
	v_max3_f32 v48, v48, v32, v33
	v_max_f32_e32 v48, v48, v50
	v_mov_b32_e32 v50, v48
	s_nop 1
	v_permlane32_swap_b32_e32 v48, v50
	v_max_f32_e32 v48, v48, v50
	v_fmamk_f32 v48, v48, 0x3fb8aa3b, v34
	v_pk_fma_f32 v[18:19], v[18:19], v[84:85], v[48:49] op_sel_hi:[1,0,0] neg_lo:[0,0,1] neg_hi:[0,0,1]
	v_exp_f32_e32 v18, v18
	v_exp_f32_e32 v19, v19
	v_pk_fma_f32 v[20:21], v[20:21], v[84:85], v[48:49] op_sel_hi:[1,0,0] neg_lo:[0,0,1] neg_hi:[0,0,1]
	v_exp_f32_e32 v20, v20
	v_exp_f32_e32 v21, v21
	v_pk_fma_f32 v[22:23], v[22:23], v[84:85], v[48:49] op_sel_hi:[1,0,0] neg_lo:[0,0,1] neg_hi:[0,0,1]
	v_exp_f32_e32 v22, v22
	v_exp_f32_e32 v23, v23
	v_pk_fma_f32 v[24:25], v[24:25], v[84:85], v[48:49] op_sel_hi:[1,0,0] neg_lo:[0,0,1] neg_hi:[0,0,1]
	v_exp_f32_e32 v24, v24
	v_exp_f32_e32 v25, v25
	v_pk_fma_f32 v[26:27], v[26:27], v[84:85], v[48:49] op_sel_hi:[1,0,0] neg_lo:[0,0,1] neg_hi:[0,0,1]
	v_exp_f32_e32 v26, v26
	v_exp_f32_e32 v27, v27
	v_pk_fma_f32 v[28:29], v[28:29], v[84:85], v[48:49] op_sel_hi:[1,0,0] neg_lo:[0,0,1] neg_hi:[0,0,1]
	v_exp_f32_e32 v28, v28
	v_exp_f32_e32 v29, v29
	v_pk_fma_f32 v[30:31], v[30:31], v[84:85], v[48:49] op_sel_hi:[1,0,0] neg_lo:[0,0,1] neg_hi:[0,0,1]
	v_exp_f32_e32 v30, v30
	v_exp_f32_e32 v31, v31
	v_pk_fma_f32 v[32:33], v[32:33], v[84:85], v[48:49] op_sel_hi:[1,0,0] neg_lo:[0,0,1] neg_hi:[0,0,1]
	v_exp_f32_e32 v32, v32
	v_exp_f32_e32 v33, v33
	v_pk_add_f32 v[56:57], v[18:19], v[20:21]
	v_pk_add_f32 v[58:59], v[22:23], v[24:25]
	v_pk_add_f32 v[60:61], v[26:27], v[28:29]
	v_pk_add_f32 v[62:63], v[30:31], v[32:33]
	v_pk_add_f32 v[56:57], v[56:57], v[58:59]
	v_pk_add_f32 v[60:61], v[60:61], v[62:63]
	v_pk_add_f32 v[56:57], v[56:57], v[60:61]
	v_add_f32_e32 v50, v56, v57
	v_mov_b32_e32 v51, v50
	s_nop 1
	v_permlane32_swap_b32_e32 v50, v51
	v_add_f32_e32 v50, v50, v51
	v_log_f32_e32 v50, v50
	v_cvt_pk_f16_f32 v40, v18, v19
	v_cvt_pk_f16_f32 v41, v20, v21
	v_cvt_pk_f16_f32 v42, v22, v23
	v_cvt_pk_f16_f32 v43, v24, v25
	v_cvt_pk_f16_f32 v44, v26, v27
	v_cvt_pk_f16_f32 v45, v28, v29
	v_cvt_pk_f16_f32 v46, v30, v31
	v_cvt_pk_f16_f32 v47, v32, v33
	v_add_f32_e32 v50, 0x41600000, v50
	v_mul_f32_e32 v50, 0xbf317218, v50
	v_cndmask_b32_e64 v51, v50, 1.0, vcc
	s_waitcnt vmcnt(0)
	ds_read_b128 v[2:5], v39
	ds_read_b128 v[6:9], v81
	ds_read_b128 v[10:13], v82
	ds_read_b128 v[14:17], v83
	s_waitcnt lgkmcnt(2)
	v_max3_f32 v52, v2, v3, v4
	v_max3_f32 v53, v5, v6, v7
	v_max_f32_e32 v52, v52, v8
	v_max_f32_e32 v53, v53, v9
	s_waitcnt lgkmcnt(0)
	v_max3_f32 v52, v52, v10, v11
	v_max3_f32 v53, v53, v12, v13
	v_max3_f32 v52, v52, v14, v15
	v_max3_f32 v53, v53, v16, v17
	v_max_f32_e32 v52, v52, v53
	v_mov_b32_e32 v53, v52
	s_nop 1
	v_permlane32_swap_b32_e32 v52, v53
	v_max_f32_e32 v52, v52, v53
	v_cndmask_b32_e32 v54, 1.0, v52, vcc
	v_fmamk_f32 v48, v52, 0x3fb8aa3b, v34
	v_pk_fma_f32 v[2:3], v[2:3], v[84:85], v[48:49] op_sel_hi:[1,0,0] neg_lo:[0,0,1] neg_hi:[0,0,1]
	v_mfma_f32_32x32x2_f32 v[64:79], v54, v51, 0
	v_exp_f32_e32 v2, v2
	v_exp_f32_e32 v3, v3
	v_pk_fma_f32 v[4:5], v[4:5], v[84:85], v[48:49] op_sel_hi:[1,0,0] neg_lo:[0,0,1] neg_hi:[0,0,1]
	v_exp_f32_e32 v4, v4
	v_exp_f32_e32 v5, v5
	v_pk_fma_f32 v[6:7], v[6:7], v[84:85], v[48:49] op_sel_hi:[1,0,0] neg_lo:[0,0,1] neg_hi:[0,0,1]
	v_exp_f32_e32 v6, v6
	v_exp_f32_e32 v7, v7
	v_pk_fma_f32 v[8:9], v[8:9], v[84:85], v[48:49] op_sel_hi:[1,0,0] neg_lo:[0,0,1] neg_hi:[0,0,1]
	v_exp_f32_e32 v8, v8
	v_exp_f32_e32 v9, v9
	v_pk_fma_f32 v[10:11], v[10:11], v[84:85], v[48:49] op_sel_hi:[1,0,0] neg_lo:[0,0,1] neg_hi:[0,0,1]
	v_exp_f32_e32 v10, v10
	v_cvt_pk_f16_f32 v56, v2, v3
	v_cvt_pk_f16_f32 v57, v4, v5
	v_cvt_pk_f16_f32 v58, v6, v7
	v_cvt_pk_f16_f32 v59, v8, v9
	v_exp_f32_e32 v11, v11
	v_pk_fma_f32 v[12:13], v[12:13], v[84:85], v[48:49] op_sel_hi:[1,0,0] neg_lo:[0,0,1] neg_hi:[0,0,1]
	v_exp_f32_e32 v12, v12
	v_mfma_f32_32x32x16_f16 v[18:33], v[56:59], v[40:43], 0
	v_exp_f32_e32 v13, v13
	v_pk_fma_f32 v[14:15], v[14:15], v[84:85], v[48:49] op_sel_hi:[1,0,0] neg_lo:[0,0,1] neg_hi:[0,0,1]
	v_exp_f32_e32 v14, v14
	v_exp_f32_e32 v15, v15
	v_pk_fma_f32 v[16:17], v[16:17], v[84:85], v[48:49] op_sel_hi:[1,0,0] neg_lo:[0,0,1] neg_hi:[0,0,1]
	v_exp_f32_e32 v16, v16
	v_exp_f32_e32 v17, v17
	v_cvt_pk_f16_f32 v60, v10, v11
	v_cvt_pk_f16_f32 v61, v12, v13
	v_cvt_pk_f16_f32 v62, v14, v15
	v_cvt_pk_f16_f32 v63, v16, v17
	s_nop 1
	v_mfma_f32_32x32x16_f16 v[18:33], v[60:63], v[44:47], v[18:33]
	s_nop 11
	v_log_f32_e32 v18, v18
	v_log_f32_e32 v19, v19
	v_log_f32_e32 v20, v20
	v_log_f32_e32 v21, v21
	v_log_f32_e32 v22, v22
	v_log_f32_e32 v23, v23
	v_pk_fma_f32 v[64:65], v[18:19], v[84:85], v[64:65] op_sel:[0,1,0] op_sel_hi:[1,1,1]
	buffer_store_dword v64, v36, s[8:11], 0 offen sc0 sc1
	buffer_store_dword v65, v36, s[8:11], s24 offen sc0 sc1
	v_log_f32_e32 v24, v24
	v_log_f32_e32 v25, v25
	v_pk_fma_f32 v[66:67], v[20:21], v[84:85], v[66:67] op_sel:[0,1,0] op_sel_hi:[1,1,1]
	buffer_store_dword v66, v36, s[8:11], s25 offen sc0 sc1
	buffer_store_dword v67, v36, s[8:11], s26 offen sc0 sc1
	v_log_f32_e32 v26, v26
	v_log_f32_e32 v27, v27
	v_pk_fma_f32 v[68:69], v[22:23], v[84:85], v[68:69] op_sel:[0,1,0] op_sel_hi:[1,1,1]
	buffer_store_dword v68, v36, s[8:11], s27 offen sc0 sc1
	buffer_store_dword v69, v36, s[8:11], s28 offen sc0 sc1
	v_log_f32_e32 v28, v28
	v_log_f32_e32 v29, v29
	v_pk_fma_f32 v[70:71], v[24:25], v[84:85], v[70:71] op_sel:[0,1,0] op_sel_hi:[1,1,1]
	buffer_store_dword v70, v36, s[8:11], s29 offen sc0 sc1
	buffer_store_dword v71, v36, s[8:11], s30 offen sc0 sc1
	v_log_f32_e32 v30, v30
	v_log_f32_e32 v31, v31
	v_pk_fma_f32 v[72:73], v[26:27], v[84:85], v[72:73] op_sel:[0,1,0] op_sel_hi:[1,1,1]
	buffer_store_dword v72, v36, s[8:11], s31 offen sc0 sc1
	buffer_store_dword v73, v36, s[8:11], s32 offen sc0 sc1
	v_log_f32_e32 v32, v32
	v_log_f32_e32 v33, v33
	v_pk_fma_f32 v[74:75], v[28:29], v[84:85], v[74:75] op_sel:[0,1,0] op_sel_hi:[1,1,1]
	buffer_store_dword v74, v36, s[8:11], s33 offen sc0 sc1
	buffer_store_dword v75, v36, s[8:11], s34 offen sc0 sc1
	v_pk_fma_f32 v[76:77], v[30:31], v[84:85], v[76:77] op_sel:[0,1,0] op_sel_hi:[1,1,1]
	buffer_store_dword v76, v36, s[8:11], s35 offen sc0 sc1
	buffer_store_dword v77, v36, s[8:11], s36 offen sc0 sc1
	v_pk_fma_f32 v[78:79], v[32:33], v[84:85], v[78:79] op_sel:[0,1,0] op_sel_hi:[1,1,1]
	buffer_store_dword v78, v36, s[8:11], s37 offen sc0 sc1
	buffer_store_dword v79, v36, s[8:11], s38 offen sc0 sc1
	s_endpgm
